# all accepted edits combined: + softmax row-sum on two accumulators and loop-invariant ALiBi A-operand zeros in the attention tile loops (on top of the packed SwiGLU epilogue version)
# speedup vs baseline: 1.0082x; 1.0024x over previous
.Lw_win_4_done:
.LBB0_519:
	s_cmp_eq_u32 s32, 0
	s_cselect_b32 s84, 0, 1
	s_sub_u32 s32, s32, s84
	s_add_i32 s2, s29, s22
	s_add_i32 s3, s27, s21
	s_add_i32 s3, s3, -1
	s_and_b32 s31, s30, 0xc000
	s_add_i32 s33, s31, 0
	s_ashr_i32 s3, s3, 2
	s_add_i32 s31, s2, 0x7e0
	s_cmp_gt_i32 s31, s23
	v_cvt_f32_i32_e32 v111, s3
	s_cselect_b64 s[34:35], -1, 0
	s_add_i32 s3, s2, 0x7ff
	s_cmp_lt_i32 s3, s24
	s_cselect_b64 s[38:39], -1, 0
	v_add_u32_e32 v2, s33, v101
	v_add_u32_e32 v4, s33, v102
	v_add_u32_e32 v5, s33, v103
	v_add_u32_e32 v6, s33, v104
	s_or_b64 s[34:35], s[34:35], s[38:39]
	s_and_b64 vcc, exec, s[34:35]
	v_add_u32_e32 v115, v2, v100
	v_add_u32_e32 v114, v4, v100
	v_add_u32_e32 v113, v5, v100
	v_add_u32_e32 v112, v6, v100
	v_add_u32_e32 v16, s33, v105
	v_add_u32_e32 v17, s33, v106
	s_barrier
	s_cbranch_vccnz .LBB0_527
	ds_read_b128 v[4:7], v115 offset:4096
	ds_read_b128 v[188:191], v114 offset:4096
	ds_read_b128 v[192:195], v113 offset:4096
	ds_read_b128 v[202:205], v112 offset:4096
	s_and_b32 s31, s31, 0xe0
	v_or_b32_e32 v2, s31, v99
	v_cvt_f32_ubyte0_e32 v2, v2
	v_and_b32_e32 v2, 0x7fff0000, v2
	v_or_b32_sdwa v2, v2, v111 dst_sel:DWORD dst_unused:UNUSED_PAD src0_sel:DWORD src1_sel:WORD_1
	v_cndmask_b32_e64 v246, 0, v2, s[36:37]
	s_cmp_ge_i32 s20, s3
	s_cselect_b64 s[34:35], -1, 0
	s_waitcnt lgkmcnt(3)
	v_mfma_f32_32x32x16_bf16 v[50:65], v[4:7], v[74:77], 0
	s_sub_i32 s3, s19, 32
	s_cmpk_lt_i32 s3, 0x1e1
	v_add3_u32 v116, v17, v94, s69
	s_cselect_b64 s[38:39], -1, 0
	s_and_b64 s[34:35], s[34:35], s[38:39]
	s_and_b64 vcc, exec, s[34:35]
	s_waitcnt lgkmcnt(2)
	v_mfma_f32_32x32x16_bf16 v[50:65], v[188:191], v[66:69], v[50:65]
	s_waitcnt lgkmcnt(1)
	v_mfma_f32_32x32x16_bf16 v[50:65], v[192:195], v[70:73], v[50:65]
	s_waitcnt lgkmcnt(0)
	v_mfma_f32_32x32x16_bf16 v[50:65], v[202:205], v[78:81], v[50:65]
	v_mfma_f32_32x32x16_bf16 v[50:65], v[246:249], v[82:85], v[50:65]
	v_add3_u32 v2, v16, v94, s69
	ds_read_b64_tr_b16 v[86:87], v2
	ds_read_b64_tr_b16 v[88:89], v2 offset:1024
	ds_read_b64_tr_b16 v[12:13], v116
	ds_read_b64_tr_b16 v[14:15], v116 offset:1024
	ds_read_b64_tr_b16 v[8:9], v2 offset:2048
	ds_read_b64_tr_b16 v[10:11], v2 offset:3072
	ds_read_b64_tr_b16 v[4:5], v116 offset:2048
	ds_read_b64_tr_b16 v[6:7], v116 offset:3072
	s_cbranch_vccnz .LBB0_524
	v_add_u32_e32 v2, s19, v108
	v_subrev_u32_e32 v116, 32, v2
	v_cmp_gt_u32_e32 vcc, s79, v116
	v_add3_u32 v116, v109, s22, 32
	s_nop 5
	v_cndmask_b32_e32 v50, v197, v50, vcc
	v_cmp_lt_u32_e32 vcc, s80, v116
	v_subrev_u32_e32 v116, 34, v2
	s_nop 0
	v_cndmask_b32_e32 v51, v197, v51, vcc
	v_cmp_gt_u32_e32 vcc, s79, v116
	v_subrev_u32_e32 v116, 35, v2
	s_nop 0
	v_cndmask_b32_e32 v52, v197, v52, vcc
	v_cmp_gt_u32_e32 vcc, s79, v116
	v_subrev_u32_e32 v116, 40, v2
	s_nop 0
	v_cndmask_b32_e32 v53, v197, v53, vcc
	v_cmp_gt_u32_e32 vcc, s79, v116
	v_subrev_u32_e32 v116, 41, v2
	s_nop 0
	v_cndmask_b32_e32 v54, v197, v54, vcc
	v_cmp_gt_u32_e32 vcc, s79, v116
	v_subrev_u32_e32 v116, 42, v2
	s_nop 0
	v_cndmask_b32_e32 v55, v197, v55, vcc
	v_cmp_gt_u32_e32 vcc, s79, v116
	v_subrev_u32_e32 v116, 43, v2
	s_nop 0
	v_cndmask_b32_e32 v56, v197, v56, vcc
	v_cmp_gt_u32_e32 vcc, s79, v116
	v_subrev_u32_e32 v116, 48, v2
	s_nop 0
	v_cndmask_b32_e32 v57, v197, v57, vcc
	v_cmp_gt_u32_e32 vcc, s79, v116
	v_subrev_u32_e32 v116, 49, v2
	s_nop 0
	v_cndmask_b32_e32 v58, v197, v58, vcc
	v_cmp_gt_u32_e32 vcc, s79, v116
	v_subrev_u32_e32 v116, 50, v2
	s_nop 0
	v_cndmask_b32_e32 v59, v197, v59, vcc
	v_cmp_gt_u32_e32 vcc, s79, v116
	v_subrev_u32_e32 v116, 51, v2
	s_nop 0
	v_cndmask_b32_e32 v60, v197, v60, vcc
	v_cmp_gt_u32_e32 vcc, s79, v116
	v_subrev_u32_e32 v116, 56, v2
	s_nop 0
	v_cndmask_b32_e32 v61, v197, v61, vcc
	v_cmp_gt_u32_e32 vcc, s79, v116
	v_subrev_u32_e32 v116, 57, v2
	s_nop 0
	v_cndmask_b32_e32 v62, v197, v62, vcc
	v_cmp_gt_u32_e32 vcc, s79, v116
	v_subrev_u32_e32 v116, 58, v2
	v_subrev_u32_e32 v2, 59, v2
	v_cndmask_b32_e32 v63, v197, v63, vcc
	v_cmp_gt_u32_e32 vcc, s79, v116
	s_nop 1
	v_cndmask_b32_e32 v64, v197, v64, vcc
	v_cmp_gt_u32_e32 vcc, s79, v2
	s_nop 1
	v_cndmask_b32_e32 v65, v197, v65, vcc

.LBB0_527:
	s_cmp_gt_i32 s25, s17
	s_cbranch_scc1 .Lring_issue_skip_0
	s_add_i32 s85, s2, 0x700
	s_mul_hi_i32 s86, s85, 0x3600
	s_mulk_i32 s85, 0x3600
	s_add_u32 s88, s12, s85
	s_addc_u32 s89, s13, s86
	s_add_u32 s90, s14, s85
	s_addc_u32 s91, s15, s86
	s_add_i32 s85, s30, 0xc000
	s_and_b32 s85, s85, 0xc000
	v_add_u32_e32 v151, s85, v97
	v_mov_b32_e32 v150, v95
	v_readfirstlane_b32 s85, v151
	v_add_u32_e32 v151, 0x2000, v151
	s_mov_b32 m0, s85
	v_readfirstlane_b32 s85, v151
	global_load_lds_dwordx4 v150, s[88:89]
	v_mov_b32_e32 v150, v96
	s_mov_b32 m0, s85
	s_nop 0
	global_load_lds_dwordx4 v150, s[90:91]

.Lw_swa_4_done:
.LBB0_780:
	s_cmp_eq_u32 s32, 0
	s_cselect_b32 s84, 0, 1
	s_sub_u32 s32, s32, s84
	s_add_i32 s0, s25, s17
	s_add_i32 s1, s23, s18
	s_add_i32 s1, s1, -1
	s_and_b32 s27, s26, 0xc000
	s_add_i32 s34, s27, 0
	s_ashr_i32 s1, s1, 2
	s_add_i32 s27, s0, 0x7e0
	s_cmp_gt_i32 s27, s19
	v_cvt_f32_i32_e32 v114, s1
	s_cselect_b64 s[28:29], -1, 0
	s_add_i32 s1, s0, 0x7ff
	s_cmp_lt_i32 s1, s20
	s_cselect_b64 s[30:31], -1, 0
	v_add_u32_e32 v2, s34, v104
	v_add_u32_e32 v4, s34, v105
	v_add_u32_e32 v5, s34, v106
	v_add_u32_e32 v6, s34, v107
	s_or_b64 s[28:29], s[28:29], s[30:31]
	s_and_b64 vcc, exec, s[28:29]
	v_add_u32_e32 v118, v2, v103
	v_add_u32_e32 v117, v4, v103
	v_add_u32_e32 v116, v5, v103
	v_add_u32_e32 v115, v6, v103
	v_add_u32_e32 v16, s34, v109
	v_add_u32_e32 v17, s34, v110
	s_barrier
	s_cbranch_vccnz .LBB0_788
	ds_read_b128 v[4:7], v118 offset:4096
	ds_read_b128 v[188:191], v117 offset:4096
	ds_read_b128 v[192:195], v116 offset:4096
	ds_read_b128 v[202:205], v115 offset:4096
	s_and_b32 s27, s27, 0xe0
	v_or_b32_e32 v2, s27, v102
	v_cvt_f32_ubyte0_e32 v2, v2
	v_and_b32_e32 v2, 0x7fff0000, v2
	v_or_b32_sdwa v2, v2, v114 dst_sel:DWORD dst_unused:UNUSED_PAD src0_sel:DWORD src1_sel:WORD_1
	v_cndmask_b32_e64 v246, 0, v2, s[36:37]
	s_cmp_ge_i32 s16, s1
	s_cselect_b64 s[28:29], -1, 0
	s_waitcnt lgkmcnt(3)
	v_mfma_f32_32x32x16_bf16 v[50:65], v[4:7], v[66:69], 0
	s_sub_i32 s1, s15, 32
	s_cmpk_lt_i32 s1, 0x61
	v_add3_u32 v119, v17, v96, s69
	s_cselect_b64 s[30:31], -1, 0
	s_and_b64 s[28:29], s[28:29], s[30:31]
	s_and_b64 vcc, exec, s[28:29]
	s_waitcnt lgkmcnt(2)
	v_mfma_f32_32x32x16_bf16 v[50:65], v[188:191], v[70:73], v[50:65]
	s_waitcnt lgkmcnt(1)
	v_mfma_f32_32x32x16_bf16 v[50:65], v[192:195], v[74:77], v[50:65]
	s_waitcnt lgkmcnt(0)
	v_mfma_f32_32x32x16_bf16 v[50:65], v[202:205], v[78:81], v[50:65]
	v_mfma_f32_32x32x16_bf16 v[50:65], v[246:249], v[82:85], v[50:65]
	v_add3_u32 v2, v16, v96, s69
	ds_read_b64_tr_b16 v[86:87], v2
	ds_read_b64_tr_b16 v[88:89], v2 offset:1024
	ds_read_b64_tr_b16 v[12:13], v119
	ds_read_b64_tr_b16 v[14:15], v119 offset:1024
	ds_read_b64_tr_b16 v[8:9], v2 offset:2048
	ds_read_b64_tr_b16 v[10:11], v2 offset:3072
	ds_read_b64_tr_b16 v[4:5], v119 offset:2048
	ds_read_b64_tr_b16 v[6:7], v119 offset:3072
	s_cbranch_vccnz .LBB0_785
	v_add_u32_e32 v2, s15, v111
	v_subrev_u32_e32 v119, 32, v2
	v_cmp_gt_u32_e32 vcc, s71, v119
	v_add3_u32 v119, v112, s17, 32
	s_nop 5
	v_cndmask_b32_e32 v50, v197, v50, vcc
	v_cmp_lt_u32_e32 vcc, s47, v119
	v_subrev_u32_e32 v119, 34, v2
	s_nop 0
	v_cndmask_b32_e32 v51, v197, v51, vcc
	v_cmp_gt_u32_e32 vcc, s71, v119
	v_subrev_u32_e32 v119, 35, v2
	s_nop 0
	v_cndmask_b32_e32 v52, v197, v52, vcc
	v_cmp_gt_u32_e32 vcc, s71, v119
	v_subrev_u32_e32 v119, 40, v2
	s_nop 0
	v_cndmask_b32_e32 v53, v197, v53, vcc
	v_cmp_gt_u32_e32 vcc, s71, v119
	v_subrev_u32_e32 v119, 41, v2
	s_nop 0
	v_cndmask_b32_e32 v54, v197, v54, vcc
	v_cmp_gt_u32_e32 vcc, s71, v119
	v_subrev_u32_e32 v119, 42, v2
	s_nop 0
	v_cndmask_b32_e32 v55, v197, v55, vcc
	v_cmp_gt_u32_e32 vcc, s71, v119
	v_subrev_u32_e32 v119, 43, v2
	s_nop 0
	v_cndmask_b32_e32 v56, v197, v56, vcc
	v_cmp_gt_u32_e32 vcc, s71, v119
	v_subrev_u32_e32 v119, 48, v2
	s_nop 0
	v_cndmask_b32_e32 v57, v197, v57, vcc
	v_cmp_gt_u32_e32 vcc, s71, v119
	v_subrev_u32_e32 v119, 49, v2
	s_nop 0
	v_cndmask_b32_e32 v58, v197, v58, vcc
	v_cmp_gt_u32_e32 vcc, s71, v119
	v_subrev_u32_e32 v119, 50, v2
	s_nop 0
	v_cndmask_b32_e32 v59, v197, v59, vcc
	v_cmp_gt_u32_e32 vcc, s71, v119
	v_subrev_u32_e32 v119, 51, v2
	s_nop 0
	v_cndmask_b32_e32 v60, v197, v60, vcc
	v_cmp_gt_u32_e32 vcc, s71, v119
	v_subrev_u32_e32 v119, 56, v2
	s_nop 0
	v_cndmask_b32_e32 v61, v197, v61, vcc
	v_cmp_gt_u32_e32 vcc, s71, v119
	v_subrev_u32_e32 v119, 57, v2
	s_nop 0
	v_cndmask_b32_e32 v62, v197, v62, vcc
	v_cmp_gt_u32_e32 vcc, s71, v119
	v_subrev_u32_e32 v119, 58, v2
	v_subrev_u32_e32 v2, 59, v2
	v_cndmask_b32_e32 v63, v197, v63, vcc
	v_cmp_gt_u32_e32 vcc, s71, v119
	s_nop 1
	v_cndmask_b32_e32 v64, v197, v64, vcc
	v_cmp_gt_u32_e32 vcc, s71, v2
	s_nop 1
	v_cndmask_b32_e32 v65, v197, v65, vcc

.LBB0_788:
	s_cmp_gt_i32 s21, s13
	s_cbranch_scc1 .Lring_issue_skip_1
	s_add_i32 s85, s0, 0x700
	s_mul_hi_i32 s86, s85, 0x3600
	s_mulk_i32 s85, 0x3600
	s_add_u32 s88, s2, s85
	s_addc_u32 s89, s3, s86
	s_add_u32 s90, s10, s85
	s_addc_u32 s91, s11, s86
	s_add_i32 s85, s26, 0xc000
	s_and_b32 s85, s85, 0xc000
	v_add_u32_e32 v151, s85, v99
	v_mov_b32_e32 v150, v97
	v_readfirstlane_b32 s85, v151
	v_add_u32_e32 v151, 0x2000, v151
	s_mov_b32 m0, s85
	v_readfirstlane_b32 s85, v151
	global_load_lds_dwordx4 v150, s[88:89]
	v_mov_b32_e32 v150, v98
	s_mov_b32 m0, s85
	s_nop 0
	global_load_lds_dwordx4 v150, s[90:91]
